# v056 + remaining statically safe LDS-DMA loads (gathered-row expert GEMM loop, prologues) in saddr form
# speedup vs baseline: 1.0043x; 1.0043x over previous
; #define PK4(P, BASE, OUT) do { u32x4 w = {cvtpk(P[BASE + 0], P[BASE + 1]), cvtpk(P[BASE + 2], P[BASE + 3]), cvtpk(P[BASE + 4], P[BASE + 5]), cvtpk(P[BASE + 6], P[BASE + 7])}; \
;     OUT = *reinterpret_cast<bf16x8*>(&w); } while (0)
; #define DMA_KP(KB, tile, b) do { _Pragma("unroll") for (int _j = 0; _j < NKW; ++_j) glds16((const char*)(KB) + (size_t)(tile) * (KVBLK * LDK * 2) + koff[_j], (LAS unsigned*)(ldsL + (b) * SHM_K + (wid * NKW + _j) * 1024)); } while (0)
; #define DMA_VP(VB, tile, b) do { _Pragma("unroll") for (int _j = 0; _j < 2; ++_j) glds16((const char*)(VB) + (size_t)(tile) * (KVBLK * LDV * 2) + voff[_j], (LAS unsigned*)(ldsL + 3 * SHM_K + (b) * SHM_V + (wid * 2 + _j) * 1024)); } while (0)
; __device__ __forceinline__ void smax_tile(f32x16& p0, f32x16& p1, float& mhat, float& l_reg, f32x16 (&o)[4], float* al_l, const bool first, int r32, int hi,
;                                           bf16x8& pa0, bf16x8& pa1, bf16x8& pa2, bf16x8& pa3) {
;     ...
; #pragma unroll
;     for (int r = 0; r < 16; ++r) p0[r] = __builtin_amdgcn_exp2f(p0[r]);
; #pragma unroll
;     for (int r = 0; r < 16; ++r) p1[r] = __builtin_amdgcn_exp2f(p1[r]);
;     float ps = p0[0];
; #pragma unroll
;     for (int r = 1; r < 16; ++r) ps += p0[r];
; #pragma unroll
;     for (int r = 0; r < 16; ++r) ps += p1[r];
;     { auto rr = __builtin_amdgcn_permlane32_swap(__float_as_uint(ps), __float_as_uint(ps), false, false); ps = __uint_as_float(rr[0]) + __uint_as_float(rr[1]); }
;     l_reg += ps;
;     ...
;     PK4(p0, 0, pa0); PK4(p0, 8, pa1); PK4(p1, 0, pa2); PK4(p1, 8, pa3);
;     ...
;     if (nxt_ && g == 1) { DMA_KP(nKh, 0, 0); DMA_KP(nKh, 1, 1); DMA_VP(nVh, 0, 0); TOUCH_Q(); }
;     SEG_S(NT - 1);
;     if (nxt_ && g == 0) { DMA_KP(nKh, 0, 0); DMA_KP(nKh, 1, 1); DMA_VP(nVh, 0, 0); TOUCH_Q(); }
.LBB0_624:
	v_exp_f32_e32 v96, v96
	v_exp_f32_e32 v97, v97
	v_exp_f32_e32 v98, v98
	v_exp_f32_e32 v99, v99
	v_exp_f32_e32 v100, v100
	v_exp_f32_e32 v101, v101
	v_exp_f32_e32 v123, v108
	v_add_f32_e32 v108, v97, v96
	v_exp_f32_e32 v102, v102
	v_add_f32_e32 v108, v98, v108
	v_exp_f32_e32 v103, v103
	v_add_f32_e32 v108, v99, v108
	v_exp_f32_e32 v104, v104
	v_add_f32_e32 v108, v100, v108
	v_exp_f32_e32 v105, v105
	v_add_f32_e32 v108, v101, v108
	v_exp_f32_e32 v106, v106
	v_add_f32_e32 v108, v102, v108
	v_exp_f32_e32 v107, v107
	v_add_f32_e32 v108, v103, v108
	v_add_f32_e32 v108, v104, v108
	v_exp_f32_e32 v124, v109
	v_add_f32_e32 v108, v105, v108
	v_exp_f32_e32 v125, v110
	v_add_f32_e32 v108, v106, v108
	v_exp_f32_e32 v126, v111
	v_add_f32_e32 v108, v107, v108
	v_exp_f32_e32 v80, v80
	v_add_f32_e32 v108, v123, v108
	v_exp_f32_e32 v81, v81
	v_add_f32_e32 v108, v124, v108
	v_exp_f32_e32 v82, v82
	v_add_f32_e32 v108, v125, v108
	v_exp_f32_e32 v83, v83
	v_add_f32_e32 v108, v126, v108
	v_exp_f32_e32 v84, v84
	v_add_f32_e32 v108, v80, v108
	v_exp_f32_e32 v85, v85
	v_add_f32_e32 v108, v81, v108
	v_exp_f32_e32 v86, v86
	v_add_f32_e32 v108, v82, v108
	v_exp_f32_e32 v87, v87
	v_add_f32_e32 v108, v83, v108
	v_exp_f32_e32 v88, v88
	v_add_f32_e32 v108, v84, v108
	v_exp_f32_e32 v89, v89
	v_add_f32_e32 v108, v85, v108
	v_exp_f32_e32 v90, v90
	v_add_f32_e32 v108, v86, v108
	v_exp_f32_e32 v91, v91
	v_add_f32_e32 v108, v87, v108
	v_exp_f32_e32 v92, v92
	v_add_f32_e32 v108, v88, v108
	v_exp_f32_e32 v93, v93
	v_add_f32_e32 v108, v89, v108
	v_exp_f32_e32 v94, v94
	v_add_f32_e32 v108, v90, v108
	v_exp_f32_e32 v95, v95
	v_add_f32_e32 v108, v91, v108
	v_add_f32_e32 v108, v92, v108
	v_add_f32_e32 v108, v93, v108
	v_add_f32_e32 v108, v94, v108
	v_add_f32_e32 v108, v95, v108
	v_mov_b32_e32 v109, v108
	s_nop 1
	v_permlane32_swap_b32_e32 v108, v109
	v_add_f32_e32 v108, v108, v109
	v_add_f32_e32 v122, v204, v108
	v_cvt_pk_bf16_f32 v108, v96, v97
	v_cvt_pk_bf16_f32 v109, v98, v99
	v_cvt_pk_bf16_f32 v110, v100, v101
	v_cvt_pk_bf16_f32 v111, v102, v103
	v_cvt_pk_bf16_f32 v104, v104, v105
	v_cvt_pk_bf16_f32 v105, v106, v107
	v_cvt_pk_bf16_f32 v106, v123, v124
	v_cvt_pk_bf16_f32 v107, v125, v126
	v_cvt_pk_bf16_f32 v100, v80, v81
	v_cvt_pk_bf16_f32 v101, v82, v83
	v_cvt_pk_bf16_f32 v102, v84, v85
	v_cvt_pk_bf16_f32 v103, v86, v87
	v_cvt_pk_bf16_f32 v96, v88, v89
	v_cvt_pk_bf16_f32 v97, v90, v91
	v_cvt_pk_bf16_f32 v98, v92, v93
	v_cvt_pk_bf16_f32 v99, v94, v95
	s_cmp_eq_u32 s92, 0
	s_cselect_b64 s[38:39], -1, 0
	s_waitcnt lgkmcnt(0)
	s_barrier
	s_and_b64 s[42:43], s[44:45], s[38:39]
	s_andn2_b64 vcc, exec, s[42:43]
	s_cbranch_vccnz .LBB0_631
	s_add_i32 s42, s73, 0
	s_mov_b32 m0, s42
	s_add_i32 s43, s74, 0
	s_add_i32 s44, s75, 0
	global_load_lds_dwordx4 v[120:121], off
	s_mov_b32 m0, s43
	s_add_u32 s36, s36, 0x18000
	global_load_lds_dwordx4 v[118:119], off
	s_mov_b32 m0, s44
	s_addc_u32 s37, s37, 0
	global_load_lds_dwordx4 v[116:117], off
	s_add_i32 m0, s42, 0x6000
	s_nop 0
	global_load_lds_dwordx4 v178, s[36:37]
	s_add_i32 m0, s43, 0x6000
	s_nop 0
	global_load_lds_dwordx4 v180, s[36:37]
	v_lshl_add_u64 v[80:81], s[36:37], 0, v[182:183]
	s_add_i32 m0, s44, 0x6000
	s_nop 0
	global_load_lds_dwordx4 v[80:81], off
	s_mov_b32 m0, s76
	s_nop 0
	global_load_lds_dwordx4 v[114:115], off
	s_add_i32 m0, s76, 0x400
	s_cmp_eq_u64 s[34:35], 0
	global_load_lds_dwordx4 v[112:113], off
	s_cbranch_scc1 .LBB0_631
	v_cmp_gt_i32_e32 vcc, s86, v200
	s_and_saveexec_b64 s[36:37], vcc
	s_cbranch_execz .LBB0_628
	v_mul_hi_i32 v80, v200, s88
	v_lshrrev_b32_e32 v81, 31, v80
	v_add_u32_e32 v82, v80, v81
	v_add_u32_e32 v83, s57, v82
	v_lshl_add_u32 v82, v82, 1, v82
	v_sub_u32_e32 v82, v200, v82
	v_mov_b64_e32 v[80:81], s[34:35]
	v_lshlrev_b32_e32 v82, 7, v82
	v_mad_i64_i32 v[80:81], s[42:43], v83, s83, v[80:81]
	v_ashrrev_i32_e32 v83, 31, v82
	v_lshl_add_u64 v[80:81], v[80:81], 0, v[82:83]
	s_add_i32 m0, s66, 0x1f000
	s_nop 0
	global_load_lds_dword v[80:81], off
